# speedup vs baseline: 1.0136x; 1.0136x over previous
_Z11edge_kernelILi36ELb1EEvPKfS1_PKDF16_PKiS5_S1_S1_S1_S1_S1_PDF16_:
	s_load_dwordx8 s[4:11], s[0:1], 0x0
	s_load_dwordx8 s[12:19], s[0:1], 0x20
	s_load_dwordx4 s[20:23], s[0:1], 0x40
	s_load_dwordx2 s[24:25], s[0:1], 0x50
	v_readfirstlane_b32 s3, v0
	v_bfe_u32 v75, v0, 4, 2
	v_and_b32_e32 v76, 15, v0
	v_and_b32_e32 v78, 63, v0
	s_lshr_b32 s3, s3, 6
	s_lshl_b32 s2, s2, 1
	s_add_i32 s2, s2, s3
	v_lshlrev_b32_e32 v74, 8, v75
	v_lshl_or_b32 v74, v76, 4, v74
	v_lshlrev_b32_e32 v79, 4, v78
	v_lshl_or_b32 v77, v76, 2, v75
	v_lshlrev_b32_e32 v77, 2, v77
	v_mul_u32_u24_e32 v73, 0x900, v75
	v_lshl_or_b32 v73, v76, 4, v73
	v_mul_u32_u24_e32 v78, 36, v75
	s_mul_i32 s28, s2, 0x2400
	s_lshl_b32 s29, s2, 14
	s_lshl_b32 s30, s2, 2
	s_lshl_b32 s31, s2, 8
	s_lshl_b32 s33, s3, 10
	s_lshl_b32 s34, s3, 8
	s_addk_i32 s34, 0x4000
	s_waitcnt lgkmcnt(0)
	s_add_u32 s10, s10, s30
	s_addc_u32 s11, s11, 0
	s_add_u32 s12, s12, s30
	s_addc_u32 s13, s13, 0
	s_load_dword s35, s[10:11], 0x0
	s_load_dword s36, s[12:13], 0x0
	s_add_u32 s14, s14, s28
	s_addc_u32 s15, s15, 0
	global_load_dwordx4 v[0:3], v73, s[14:15] nt
	global_load_dwordx4 v[4:7], v73, s[14:15] offset:256 nt
	global_load_dwordx4 v[8:11], v73, s[14:15] offset:512 nt
	global_load_dwordx4 v[12:15], v73, s[14:15] offset:768 nt
	global_load_dwordx4 v[16:19], v73, s[14:15] offset:1024 nt
	global_load_dwordx4 v[20:23], v73, s[14:15] offset:1280 nt
	global_load_dwordx4 v[24:27], v73, s[14:15] offset:1536 nt
	global_load_dwordx4 v[28:31], v73, s[14:15] offset:1792 nt
	global_load_dwordx4 v[32:35], v73, s[14:15] offset:2048 nt
	s_add_u32 s22, s22, s33
	s_addc_u32 s23, s23, 0
	s_add_u32 s18, s18, s29
	s_addc_u32 s19, s19, 0
	s_mov_b32 m0, s33
	s_nop 0
	global_load_lds_dwordx4 v79, s[22:23]
	global_load_lds_dwordx4 v79, s[22:23] offset:2048
	s_add_u32 m0, m0, 0x1000
	s_add_u32 s22, s22, 0x1000
	s_addc_u32 s23, s23, 0
	global_load_lds_dwordx4 v79, s[22:23]
	global_load_lds_dwordx4 v79, s[22:23] offset:2048
	s_add_u32 m0, m0, 0x1000
	s_add_u32 s22, s22, 0x1000
	s_addc_u32 s23, s23, 0
	global_load_lds_dwordx4 v79, s[22:23]
	global_load_lds_dwordx4 v79, s[22:23] offset:2048
	s_add_u32 m0, m0, 0x1000
	s_add_u32 s22, s22, 0x1000
	s_addc_u32 s23, s23, 0
	global_load_lds_dwordx4 v79, s[22:23]
	global_load_lds_dwordx4 v79, s[22:23] offset:2048
	s_add_u32 s16, s16, s31
	s_addc_u32 s17, s17, 0
	s_add_u32 s20, s20, s31
	s_addc_u32 s21, s21, 0
	s_waitcnt lgkmcnt(0)
	s_lshl_b32 s36, s36, 7
	s_add_u32 s24, s24, s36
	s_addc_u32 s25, s25, 0
	s_lshl_b32 s37, s35, 7
	s_lshl_b32 s38, s35, 4
	s_add_u32 s4, s4, s37
	s_addc_u32 s5, s5, 0
	s_add_u32 s6, s6, s38
	s_addc_u32 s7, s7, 0
	v_mov_b32_e32 v93, 0
	v_mov_b32_e32 v92, v78
	v_lshl_add_u64 v[94:95], s[4:5], 0, v[92:93]
	v_lshl_add_u64 v[94:95], v[94:95], 0, 20
	v_cmp_eq_u32_e32 vcc, 3, v75
	s_nop 1
	v_mov_b32_e32 v90, s6
	v_mov_b32_e32 v91, s7
	v_cndmask_b32_e32 v94, v94, v90, vcc
	v_cndmask_b32_e32 v95, v95, v91, vcc
	global_load_dwordx4 v[80:83], v78, s[4:5] nt
	global_load_dword v84, v78, s[4:5] offset:16 nt
	global_load_dwordx4 v[86:89], v[94:95], off nt
	global_load_dword v72, v77, s[16:17] nt
	global_load_dword v64, v77, s[20:21] nt
	v_add_u32_e32 v78, s34, v77
	v_lshl_add_u32 v79, v75, 2, s34
	s_waitcnt vmcnt(2)
	s_barrier
	v_pk_mul_f32 v[96:97], v[80:81], v[0:1] op_sel_hi:[0,1]
	v_pk_mul_f32 v[98:99], v[80:81], v[2:3] op_sel_hi:[0,1]
	v_pk_mul_f32 v[100:101], v[80:81], v[4:5] op_sel:[1,0]
	v_pk_mul_f32 v[102:103], v[80:81], v[6:7] op_sel:[1,0]
	v_pk_fma_f32 v[96:97], v[82:83], v[8:9], v[96:97] op_sel_hi:[0,1,1]
	v_pk_fma_f32 v[98:99], v[82:83], v[10:11], v[98:99] op_sel_hi:[0,1,1]
	v_pk_fma_f32 v[100:101], v[82:83], v[12:13], v[100:101] op_sel:[1,0,0]
	v_pk_fma_f32 v[102:103], v[82:83], v[14:15], v[102:103] op_sel:[1,0,0]
	v_pk_fma_f32 v[96:97], v[84:85], v[16:17], v[96:97] op_sel_hi:[0,1,1]
	v_pk_fma_f32 v[98:99], v[84:85], v[18:19], v[98:99] op_sel_hi:[0,1,1]
	v_pk_fma_f32 v[100:101], v[86:87], v[20:21], v[100:101] op_sel_hi:[0,1,1]
	v_pk_fma_f32 v[102:103], v[86:87], v[22:23], v[102:103] op_sel_hi:[0,1,1]
	v_pk_fma_f32 v[96:97], v[86:87], v[24:25], v[96:97] op_sel:[1,0,0]
	v_pk_fma_f32 v[98:99], v[86:87], v[26:27], v[98:99] op_sel:[1,0,0]
	v_pk_fma_f32 v[100:101], v[88:89], v[28:29], v[100:101] op_sel_hi:[0,1,1]
	v_pk_fma_f32 v[102:103], v[88:89], v[30:31], v[102:103] op_sel_hi:[0,1,1]
	v_pk_fma_f32 v[96:97], v[88:89], v[32:33], v[96:97] op_sel:[1,0,0]
	v_pk_fma_f32 v[98:99], v[88:89], v[34:35], v[98:99] op_sel:[1,0,0]
	v_pk_add_f32 v[96:97], v[96:97], v[100:101]
	v_pk_add_f32 v[98:99], v[98:99], v[102:103]
	s_nop 1
	v_permlane16_swap_b32_e32 v96, v97
	v_permlane16_swap_b32_e32 v98, v99
	v_add_f32_e32 v96, v96, v97
	v_add_f32_e32 v98, v98, v99
	s_nop 1
	v_permlane32_swap_b32_e32 v96, v98
	v_add_f32_e32 v96, v96, v98
	s_waitcnt vmcnt(1)
	v_add_f32_e32 v96, v96, v72
	v_max_f32_e32 v96, 0, v96
	ds_write_b32 v78, v96
	ds_read2_b32 v[80:81], v79 offset0:0 offset1:4
	ds_read2_b32 v[82:83], v79 offset0:8 offset1:12
	ds_read2_b32 v[84:85], v79 offset0:16 offset1:20
	ds_read2_b32 v[86:87], v79 offset0:24 offset1:28
	ds_read2_b32 v[88:89], v79 offset0:32 offset1:36
	ds_read2_b32 v[90:91], v79 offset0:40 offset1:44
	ds_read2_b32 v[92:93], v79 offset0:48 offset1:52
	ds_read2_b32 v[94:95], v79 offset0:56 offset1:60
	s_waitcnt lgkmcnt(0)
	v_cmp_neq_f32_e64 s[40:41], 0, v80
	v_cmp_neq_f32_e64 s[42:43], 0, v81
	v_cmp_neq_f32_e64 s[44:45], 0, v82
	v_cmp_neq_f32_e64 s[46:47], 0, v83
	v_cmp_neq_f32_e64 s[48:49], 0, v84
	v_cmp_neq_f32_e64 s[50:51], 0, v85
	v_cmp_neq_f32_e64 s[52:53], 0, v86
	v_cmp_neq_f32_e64 s[54:55], 0, v87
	v_cmp_neq_f32_e64 s[56:57], 0, v88
	v_cmp_neq_f32_e64 s[58:59], 0, v89
	v_cmp_neq_f32_e64 s[60:61], 0, v90
	v_cmp_neq_f32_e64 s[62:63], 0, v91
	v_cmp_neq_f32_e64 s[64:65], 0, v92
	v_cmp_neq_f32_e64 s[66:67], 0, v93
	v_cmp_neq_f32_e64 s[68:69], 0, v94
	v_cmp_neq_f32_e64 s[70:71], 0, v95
	s_mov_b64 exec, s[40:41]
	global_load_dwordx4 v[0:3], v74, s[18:19] nt
	s_mov_b64 exec, s[42:43]
	global_load_dwordx4 v[4:7], v74, s[18:19] offset:1024 nt
	s_mov_b64 exec, s[44:45]
	global_load_dwordx4 v[8:11], v74, s[18:19] offset:2048 nt
	s_mov_b64 exec, s[46:47]
	global_load_dwordx4 v[12:15], v74, s[18:19] offset:3072 nt
	s_add_u32 s18, s18, 0x1000
	s_addc_u32 s19, s19, 0
	s_mov_b64 exec, s[48:49]
	global_load_dwordx4 v[16:19], v74, s[18:19] nt
	s_mov_b64 exec, s[50:51]
	global_load_dwordx4 v[20:23], v74, s[18:19] offset:1024 nt
	s_mov_b64 exec, s[52:53]
	global_load_dwordx4 v[24:27], v74, s[18:19] offset:2048 nt
	s_mov_b64 exec, s[54:55]
	global_load_dwordx4 v[28:31], v74, s[18:19] offset:3072 nt
	s_add_u32 s18, s18, 0x1000
	s_addc_u32 s19, s19, 0
	s_mov_b64 exec, s[56:57]
	global_load_dwordx4 v[32:35], v74, s[18:19] nt
	s_mov_b64 exec, s[58:59]
	global_load_dwordx4 v[36:39], v74, s[18:19] offset:1024 nt
	s_mov_b64 exec, s[60:61]
	global_load_dwordx4 v[40:43], v74, s[18:19] offset:2048 nt
	s_mov_b64 exec, s[62:63]
	global_load_dwordx4 v[44:47], v74, s[18:19] offset:3072 nt
	s_add_u32 s18, s18, 0x1000
	s_addc_u32 s19, s19, 0
	s_mov_b64 exec, s[64:65]
	global_load_dwordx4 v[48:51], v74, s[18:19] nt
	s_mov_b64 exec, s[66:67]
	global_load_dwordx4 v[52:55], v74, s[18:19] offset:1024 nt
	s_mov_b64 exec, s[68:69]
	global_load_dwordx4 v[56:59], v74, s[18:19] offset:2048 nt
	s_mov_b64 exec, s[70:71]
	global_load_dwordx4 v[60:63], v74, s[18:19] offset:3072 nt
	s_mov_b64 exec, -1
	v_mov_b32_e32 v96, 0
	v_mov_b32_e32 v97, 0
	v_mov_b32_e32 v98, 0
	v_mov_b32_e32 v99, 0
	v_mov_b32_e32 v100, 0
	v_mov_b32_e32 v101, 0
	v_mov_b32_e32 v102, 0
	v_mov_b32_e32 v103, 0
	s_waitcnt vmcnt(0)
	s_mov_b64 exec, s[40:41]
	v_pk_fma_f32 v[96:97], v[80:81], v[0:1], v[96:97] op_sel_hi:[0,1,1]
	v_pk_fma_f32 v[98:99], v[80:81], v[2:3], v[98:99] op_sel_hi:[0,1,1]
	s_mov_b64 exec, s[42:43]
	v_pk_fma_f32 v[100:101], v[80:81], v[4:5], v[100:101] op_sel:[1,0,0]
	v_pk_fma_f32 v[102:103], v[80:81], v[6:7], v[102:103] op_sel:[1,0,0]
	s_mov_b64 exec, s[44:45]
	v_pk_fma_f32 v[96:97], v[82:83], v[8:9], v[96:97] op_sel_hi:[0,1,1]
	v_pk_fma_f32 v[98:99], v[82:83], v[10:11], v[98:99] op_sel_hi:[0,1,1]
	s_mov_b64 exec, s[46:47]
	v_pk_fma_f32 v[100:101], v[82:83], v[12:13], v[100:101] op_sel:[1,0,0]
	v_pk_fma_f32 v[102:103], v[82:83], v[14:15], v[102:103] op_sel:[1,0,0]
	s_mov_b64 exec, s[48:49]
	v_pk_fma_f32 v[96:97], v[84:85], v[16:17], v[96:97] op_sel_hi:[0,1,1]
	v_pk_fma_f32 v[98:99], v[84:85], v[18:19], v[98:99] op_sel_hi:[0,1,1]
	s_mov_b64 exec, s[50:51]
	v_pk_fma_f32 v[100:101], v[84:85], v[20:21], v[100:101] op_sel:[1,0,0]
	v_pk_fma_f32 v[102:103], v[84:85], v[22:23], v[102:103] op_sel:[1,0,0]
	s_mov_b64 exec, s[52:53]
	v_pk_fma_f32 v[96:97], v[86:87], v[24:25], v[96:97] op_sel_hi:[0,1,1]
	v_pk_fma_f32 v[98:99], v[86:87], v[26:27], v[98:99] op_sel_hi:[0,1,1]
	s_mov_b64 exec, s[54:55]
	v_pk_fma_f32 v[100:101], v[86:87], v[28:29], v[100:101] op_sel:[1,0,0]
	v_pk_fma_f32 v[102:103], v[86:87], v[30:31], v[102:103] op_sel:[1,0,0]
	s_mov_b64 exec, s[56:57]
	v_pk_fma_f32 v[96:97], v[88:89], v[32:33], v[96:97] op_sel_hi:[0,1,1]
	v_pk_fma_f32 v[98:99], v[88:89], v[34:35], v[98:99] op_sel_hi:[0,1,1]
	s_mov_b64 exec, s[58:59]
	v_pk_fma_f32 v[100:101], v[88:89], v[36:37], v[100:101] op_sel:[1,0,0]
	v_pk_fma_f32 v[102:103], v[88:89], v[38:39], v[102:103] op_sel:[1,0,0]
	s_mov_b64 exec, s[60:61]
	v_pk_fma_f32 v[96:97], v[90:91], v[40:41], v[96:97] op_sel_hi:[0,1,1]
	v_pk_fma_f32 v[98:99], v[90:91], v[42:43], v[98:99] op_sel_hi:[0,1,1]
	s_mov_b64 exec, s[62:63]
	v_pk_fma_f32 v[100:101], v[90:91], v[44:45], v[100:101] op_sel:[1,0,0]
	v_pk_fma_f32 v[102:103], v[90:91], v[46:47], v[102:103] op_sel:[1,0,0]
	s_mov_b64 exec, s[64:65]
	v_pk_fma_f32 v[96:97], v[92:93], v[48:49], v[96:97] op_sel_hi:[0,1,1]
	v_pk_fma_f32 v[98:99], v[92:93], v[50:51], v[98:99] op_sel_hi:[0,1,1]
	s_mov_b64 exec, s[66:67]
	v_pk_fma_f32 v[100:101], v[92:93], v[52:53], v[100:101] op_sel:[1,0,0]
	v_pk_fma_f32 v[102:103], v[92:93], v[54:55], v[102:103] op_sel:[1,0,0]
	s_mov_b64 exec, s[68:69]
	v_pk_fma_f32 v[96:97], v[94:95], v[56:57], v[96:97] op_sel_hi:[0,1,1]
	v_pk_fma_f32 v[98:99], v[94:95], v[58:59], v[98:99] op_sel_hi:[0,1,1]
	s_mov_b64 exec, s[70:71]
	v_pk_fma_f32 v[100:101], v[94:95], v[60:61], v[100:101] op_sel:[1,0,0]
	v_pk_fma_f32 v[102:103], v[94:95], v[62:63], v[102:103] op_sel:[1,0,0]
	s_mov_b64 exec, -1
	ds_read_b128 v[0:3], v74
	ds_read_b128 v[4:7], v74 offset:1024
	ds_read_b128 v[8:11], v74 offset:2048
	ds_read_b128 v[12:15], v74 offset:3072
	ds_read_b128 v[16:19], v74 offset:4096
	ds_read_b128 v[20:23], v74 offset:5120
	ds_read_b128 v[24:27], v74 offset:6144
	ds_read_b128 v[28:31], v74 offset:7168
	ds_read_b128 v[32:35], v74 offset:8192
	ds_read_b128 v[36:39], v74 offset:9216
	ds_read_b128 v[40:43], v74 offset:10240
	ds_read_b128 v[44:47], v74 offset:11264
	ds_read_b128 v[48:51], v74 offset:12288
	ds_read_b128 v[52:55], v74 offset:13312
	ds_read_b128 v[56:59], v74 offset:14336
	v_pk_add_f32 v[96:97], v[96:97], v[100:101]
	v_pk_add_f32 v[98:99], v[98:99], v[102:103]
	s_nop 1
	v_permlane16_swap_b32_e32 v96, v97
	v_permlane16_swap_b32_e32 v98, v99
	v_add_f32_e32 v96, v96, v97
	v_add_f32_e32 v98, v98, v99
	s_nop 1
	v_permlane32_swap_b32_e32 v96, v98
	v_add_f32_e32 v96, v96, v98
	v_add_f32_e32 v96, v96, v64
	s_waitcnt lgkmcnt(5)
	ds_read_b128 v[60:63], v74 offset:15360
	ds_write_b32 v78, v96
	ds_read2_b32 v[80:81], v79 offset0:0 offset1:4
	ds_read2_b32 v[82:83], v79 offset0:8 offset1:12
	ds_read2_b32 v[84:85], v79 offset0:16 offset1:20
	ds_read2_b32 v[86:87], v79 offset0:24 offset1:28
	ds_read2_b32 v[88:89], v79 offset0:32 offset1:36
	ds_read2_b32 v[90:91], v79 offset0:40 offset1:44
	ds_read2_b32 v[92:93], v79 offset0:48 offset1:52
	ds_read2_b32 v[94:95], v79 offset0:56 offset1:60
	v_lshlrev_b32_e32 v72, 3, v76
	v_lshl_or_b32 v72, v75, 2, v72
	v_cmp_gt_u32_e32 vcc, 2, v75
	s_waitcnt lgkmcnt(0)
	v_pk_mul_f32 v[96:97], v[80:81], v[0:1] op_sel_hi:[0,1]
	v_pk_mul_f32 v[98:99], v[80:81], v[2:3] op_sel_hi:[0,1]
	v_pk_mul_f32 v[100:101], v[80:81], v[4:5] op_sel:[1,0]
	v_pk_mul_f32 v[102:103], v[80:81], v[6:7] op_sel:[1,0]
	v_pk_fma_f32 v[96:97], v[82:83], v[8:9], v[96:97] op_sel_hi:[0,1,1]
	v_pk_fma_f32 v[98:99], v[82:83], v[10:11], v[98:99] op_sel_hi:[0,1,1]
	v_pk_fma_f32 v[100:101], v[82:83], v[12:13], v[100:101] op_sel:[1,0,0]
	v_pk_fma_f32 v[102:103], v[82:83], v[14:15], v[102:103] op_sel:[1,0,0]
	v_pk_fma_f32 v[96:97], v[84:85], v[16:17], v[96:97] op_sel_hi:[0,1,1]
	v_pk_fma_f32 v[98:99], v[84:85], v[18:19], v[98:99] op_sel_hi:[0,1,1]
	v_pk_fma_f32 v[100:101], v[84:85], v[20:21], v[100:101] op_sel:[1,0,0]
	v_pk_fma_f32 v[102:103], v[84:85], v[22:23], v[102:103] op_sel:[1,0,0]
	v_pk_fma_f32 v[96:97], v[86:87], v[24:25], v[96:97] op_sel_hi:[0,1,1]
	v_pk_fma_f32 v[98:99], v[86:87], v[26:27], v[98:99] op_sel_hi:[0,1,1]
	v_pk_fma_f32 v[100:101], v[86:87], v[28:29], v[100:101] op_sel:[1,0,0]
	v_pk_fma_f32 v[102:103], v[86:87], v[30:31], v[102:103] op_sel:[1,0,0]
	v_pk_fma_f32 v[96:97], v[88:89], v[32:33], v[96:97] op_sel_hi:[0,1,1]
	v_pk_fma_f32 v[98:99], v[88:89], v[34:35], v[98:99] op_sel_hi:[0,1,1]
	v_pk_fma_f32 v[100:101], v[88:89], v[36:37], v[100:101] op_sel:[1,0,0]
	v_pk_fma_f32 v[102:103], v[88:89], v[38:39], v[102:103] op_sel:[1,0,0]
	v_pk_fma_f32 v[96:97], v[90:91], v[40:41], v[96:97] op_sel_hi:[0,1,1]
	v_pk_fma_f32 v[98:99], v[90:91], v[42:43], v[98:99] op_sel_hi:[0,1,1]
	v_pk_fma_f32 v[100:101], v[90:91], v[44:45], v[100:101] op_sel:[1,0,0]
	v_pk_fma_f32 v[102:103], v[90:91], v[46:47], v[102:103] op_sel:[1,0,0]
	v_pk_fma_f32 v[96:97], v[92:93], v[48:49], v[96:97] op_sel_hi:[0,1,1]
	v_pk_fma_f32 v[98:99], v[92:93], v[50:51], v[98:99] op_sel_hi:[0,1,1]
	v_pk_fma_f32 v[100:101], v[92:93], v[52:53], v[100:101] op_sel:[1,0,0]
	v_pk_fma_f32 v[102:103], v[92:93], v[54:55], v[102:103] op_sel:[1,0,0]
	v_pk_fma_f32 v[96:97], v[94:95], v[56:57], v[96:97] op_sel_hi:[0,1,1]
	v_pk_fma_f32 v[98:99], v[94:95], v[58:59], v[98:99] op_sel_hi:[0,1,1]
	v_pk_fma_f32 v[100:101], v[94:95], v[60:61], v[100:101] op_sel:[1,0,0]
	v_pk_fma_f32 v[102:103], v[94:95], v[62:63], v[102:103] op_sel:[1,0,0]
	v_pk_add_f32 v[96:97], v[96:97], v[100:101]
	v_pk_add_f32 v[98:99], v[98:99], v[102:103]
	s_nop 1
	v_permlane16_swap_b32_e32 v96, v98
	v_permlane16_swap_b32_e32 v97, v99
	v_add_f32_e32 v96, v96, v98
	v_add_f32_e32 v97, v97, v99
	v_mov_b32_e32 v80, v96
	v_mov_b32_e32 v81, v97
	s_nop 1
	v_permlane32_swap_b32_e32 v96, v80
	v_permlane32_swap_b32_e32 v97, v81
	v_add_f32_e32 v96, v96, v80
	v_add_f32_e32 v97, v97, v81
	v_cvt_pk_f16_f32 v73, v96, v97
	s_and_saveexec_b64 s[4:5], vcc
	global_atomic_pk_add_f16 v72, v73, s[24:25]
	s_endpgm
	.p2align	8

_Z11edge_kernelILi64ELb0EEvPKfS1_PKDF16_PKiS5_S1_S1_S1_S1_S1_PDF16_:
	s_load_dwordx16 s[4:19], s[0:1], 0x10
	s_load_dwordx2 s[20:21], s[0:1], 0x50
	v_readfirstlane_b32 s3, v0
	v_bfe_u32 v75, v0, 4, 2
	v_and_b32_e32 v76, 15, v0
	v_and_b32_e32 v78, 63, v0
	s_lshr_b32 s3, s3, 6
	s_lshl_b32 s2, s2, 1
	s_add_i32 s2, s2, s3
	v_lshlrev_b32_e32 v74, 8, v75
	v_lshl_or_b32 v74, v76, 4, v74
	v_lshlrev_b32_e32 v79, 4, v78
	v_lshl_or_b32 v77, v76, 2, v75
	v_lshlrev_b32_e32 v77, 2, v77
	v_lshlrev_b32_e32 v78, 5, v75
	v_lshlrev_b32_e32 v73, 12, v75
	v_lshl_or_b32 v73, v76, 4, v73
	s_lshl_b32 s28, s2, 14
	s_lshl_b32 s29, s2, 14
	s_lshl_b32 s30, s2, 2
	s_lshl_b32 s31, s2, 8
	s_lshl_b32 s33, s3, 10
	s_lshl_b32 s34, s3, 8
	s_addk_i32 s34, 0x4000
	s_waitcnt lgkmcnt(0)
	s_add_u32 s6, s6, s30
	s_addc_u32 s7, s7, 0
	s_add_u32 s8, s8, s30
	s_addc_u32 s9, s9, 0
	s_load_dword s35, s[6:7], 0x0
	s_load_dword s36, s[8:9], 0x0
	s_add_u32 s10, s10, s28
	s_addc_u32 s11, s11, 0
	s_add_u32 s18, s18, s33
	s_addc_u32 s19, s19, 0
	s_add_u32 s14, s14, s29
	s_addc_u32 s15, s15, 0
	s_add_u32 s12, s12, s31
	s_addc_u32 s13, s13, 0
	s_add_u32 s16, s16, s31
	s_addc_u32 s17, s17, 0
	s_waitcnt lgkmcnt(0)
	s_lshl_b32 s36, s36, 7
	s_add_u32 s20, s20, s36
	s_addc_u32 s21, s21, 0
	s_lshl_b32 s37, s35, 7
	s_add_u32 s4, s4, s37
	s_addc_u32 s5, s5, 0
	global_load_dwordx4 v[64:67], v78, s[4:5] nt
	global_load_dwordx4 v[68:71], v78, s[4:5] offset:16 nt
	v_add_u32_e32 v78, s34, v77
	s_waitcnt vmcnt(0)
	v_cvt_f32_f16_e32 v80, v64
	v_cvt_f32_f16_sdwa v81, v64 dst_sel:DWORD dst_unused:UNUSED_PAD src0_sel:WORD_1
	v_cvt_f32_f16_e32 v82, v65
	v_cvt_f32_f16_sdwa v83, v65 dst_sel:DWORD dst_unused:UNUSED_PAD src0_sel:WORD_1
	v_cvt_f32_f16_e32 v84, v66
	v_cvt_f32_f16_sdwa v85, v66 dst_sel:DWORD dst_unused:UNUSED_PAD src0_sel:WORD_1
	v_cvt_f32_f16_e32 v86, v67
	v_cvt_f32_f16_sdwa v87, v67 dst_sel:DWORD dst_unused:UNUSED_PAD src0_sel:WORD_1
	v_cvt_f32_f16_e32 v88, v68
	v_cvt_f32_f16_sdwa v89, v68 dst_sel:DWORD dst_unused:UNUSED_PAD src0_sel:WORD_1
	v_cvt_f32_f16_e32 v90, v69
	v_cvt_f32_f16_sdwa v91, v69 dst_sel:DWORD dst_unused:UNUSED_PAD src0_sel:WORD_1
	v_cvt_f32_f16_e32 v92, v70
	v_cvt_f32_f16_sdwa v93, v70 dst_sel:DWORD dst_unused:UNUSED_PAD src0_sel:WORD_1
	v_cvt_f32_f16_e32 v94, v71
	v_cvt_f32_f16_sdwa v95, v71 dst_sel:DWORD dst_unused:UNUSED_PAD src0_sel:WORD_1
	v_max_f32_e32 v80, 0, v80
	v_max_f32_e32 v81, 0, v81
	v_max_f32_e32 v82, 0, v82
	v_max_f32_e32 v83, 0, v83
	v_max_f32_e32 v84, 0, v84
	v_max_f32_e32 v85, 0, v85
	v_max_f32_e32 v86, 0, v86
	v_max_f32_e32 v87, 0, v87
	v_max_f32_e32 v88, 0, v88
	v_max_f32_e32 v89, 0, v89
	v_max_f32_e32 v90, 0, v90
	v_max_f32_e32 v91, 0, v91
	v_max_f32_e32 v92, 0, v92
	v_max_f32_e32 v93, 0, v93
	v_max_f32_e32 v94, 0, v94
	v_max_f32_e32 v95, 0, v95
	v_cmp_neq_f32_e64 s[40:41], 0, v80
	v_cmp_neq_f32_e64 s[42:43], 0, v81
	v_cmp_neq_f32_e64 s[44:45], 0, v82
	v_cmp_neq_f32_e64 s[46:47], 0, v83
	v_cmp_neq_f32_e64 s[48:49], 0, v84
	v_cmp_neq_f32_e64 s[50:51], 0, v85
	v_cmp_neq_f32_e64 s[52:53], 0, v86
	v_cmp_neq_f32_e64 s[54:55], 0, v87
	v_cmp_neq_f32_e64 s[56:57], 0, v88
	v_cmp_neq_f32_e64 s[58:59], 0, v89
	v_cmp_neq_f32_e64 s[60:61], 0, v90
	v_cmp_neq_f32_e64 s[62:63], 0, v91
	v_cmp_neq_f32_e64 s[64:65], 0, v92
	v_cmp_neq_f32_e64 s[66:67], 0, v93
	v_cmp_neq_f32_e64 s[68:69], 0, v94
	v_cmp_neq_f32_e64 s[70:71], 0, v95
	v_lshlrev_b32_e32 v96, 12, v75
	v_lshl_or_b32 v96, v76, 4, v96
	s_mov_b64 exec, s[40:41]
	global_load_dwordx4 v[0:3], v96, s[10:11] nt
	s_mov_b64 exec, s[42:43]
	global_load_dwordx4 v[4:7], v96, s[10:11] offset:256 nt
	s_mov_b64 exec, s[44:45]
	global_load_dwordx4 v[8:11], v96, s[10:11] offset:512 nt
	s_mov_b64 exec, s[46:47]
	global_load_dwordx4 v[12:15], v96, s[10:11] offset:768 nt
	s_mov_b64 exec, s[48:49]
	global_load_dwordx4 v[16:19], v96, s[10:11] offset:1024 nt
	s_mov_b64 exec, s[50:51]
	global_load_dwordx4 v[20:23], v96, s[10:11] offset:1280 nt
	s_mov_b64 exec, s[52:53]
	global_load_dwordx4 v[24:27], v96, s[10:11] offset:1536 nt
	s_mov_b64 exec, s[54:55]
	global_load_dwordx4 v[28:31], v96, s[10:11] offset:1792 nt
	s_mov_b64 exec, s[56:57]
	global_load_dwordx4 v[32:35], v96, s[10:11] offset:2048 nt
	s_mov_b64 exec, s[58:59]
	global_load_dwordx4 v[36:39], v96, s[10:11] offset:2304 nt
	s_mov_b64 exec, s[60:61]
	global_load_dwordx4 v[40:43], v96, s[10:11] offset:2560 nt
	s_mov_b64 exec, s[62:63]
	global_load_dwordx4 v[44:47], v96, s[10:11] offset:2816 nt
	s_mov_b64 exec, s[64:65]
	global_load_dwordx4 v[48:51], v96, s[10:11] offset:3072 nt
	s_mov_b64 exec, s[66:67]
	global_load_dwordx4 v[52:55], v96, s[10:11] offset:3328 nt
	s_mov_b64 exec, s[68:69]
	global_load_dwordx4 v[56:59], v96, s[10:11] offset:3584 nt
	s_mov_b64 exec, s[70:71]
	global_load_dwordx4 v[60:63], v96, s[10:11] offset:3840 nt
	s_mov_b64 exec, -1
	s_mov_b32 m0, s33
	s_nop 0
	global_load_lds_dwordx4 v79, s[18:19]
	global_load_lds_dwordx4 v79, s[18:19] offset:2048
	s_add_u32 m0, m0, 0x1000
	s_add_u32 s18, s18, 0x1000
	s_addc_u32 s19, s19, 0
	global_load_lds_dwordx4 v79, s[18:19]
	global_load_lds_dwordx4 v79, s[18:19] offset:2048
	s_add_u32 m0, m0, 0x1000
	s_add_u32 s18, s18, 0x1000
	s_addc_u32 s19, s19, 0
	global_load_lds_dwordx4 v79, s[18:19]
	global_load_lds_dwordx4 v79, s[18:19] offset:2048
	s_add_u32 m0, m0, 0x1000
	s_add_u32 s18, s18, 0x1000
	s_addc_u32 s19, s19, 0
	global_load_lds_dwordx4 v79, s[18:19]
	global_load_lds_dwordx4 v79, s[18:19] offset:2048
	global_load_dword v72, v77, s[12:13] nt
	global_load_dword v73, v77, s[16:17] nt
	v_lshl_add_u32 v79, v75, 2, s34
	v_mov_b32_e32 v96, 0
	v_mov_b32_e32 v97, 0
	v_mov_b32_e32 v98, 0
	v_mov_b32_e32 v99, 0
	v_mov_b32_e32 v100, 0
	v_mov_b32_e32 v101, 0
	v_mov_b32_e32 v102, 0
	v_mov_b32_e32 v103, 0
	s_waitcnt vmcnt(0)
	s_barrier
	s_mov_b64 exec, s[40:41]
	v_pk_fma_f32 v[96:97], v[80:81], v[0:1], v[96:97] op_sel_hi:[0,1,1]
	v_pk_fma_f32 v[98:99], v[80:81], v[2:3], v[98:99] op_sel_hi:[0,1,1]
	s_mov_b64 exec, s[42:43]
	v_pk_fma_f32 v[100:101], v[80:81], v[4:5], v[100:101] op_sel:[1,0,0]
	v_pk_fma_f32 v[102:103], v[80:81], v[6:7], v[102:103] op_sel:[1,0,0]
	s_mov_b64 exec, s[44:45]
	v_pk_fma_f32 v[96:97], v[82:83], v[8:9], v[96:97] op_sel_hi:[0,1,1]
	v_pk_fma_f32 v[98:99], v[82:83], v[10:11], v[98:99] op_sel_hi:[0,1,1]
	s_mov_b64 exec, s[46:47]
	v_pk_fma_f32 v[100:101], v[82:83], v[12:13], v[100:101] op_sel:[1,0,0]
	v_pk_fma_f32 v[102:103], v[82:83], v[14:15], v[102:103] op_sel:[1,0,0]
	s_mov_b64 exec, s[48:49]
	v_pk_fma_f32 v[96:97], v[84:85], v[16:17], v[96:97] op_sel_hi:[0,1,1]
	v_pk_fma_f32 v[98:99], v[84:85], v[18:19], v[98:99] op_sel_hi:[0,1,1]
	s_mov_b64 exec, s[50:51]
	v_pk_fma_f32 v[100:101], v[84:85], v[20:21], v[100:101] op_sel:[1,0,0]
	v_pk_fma_f32 v[102:103], v[84:85], v[22:23], v[102:103] op_sel:[1,0,0]
	s_mov_b64 exec, s[52:53]
	v_pk_fma_f32 v[96:97], v[86:87], v[24:25], v[96:97] op_sel_hi:[0,1,1]
	v_pk_fma_f32 v[98:99], v[86:87], v[26:27], v[98:99] op_sel_hi:[0,1,1]
	s_mov_b64 exec, s[54:55]
	v_pk_fma_f32 v[100:101], v[86:87], v[28:29], v[100:101] op_sel:[1,0,0]
	v_pk_fma_f32 v[102:103], v[86:87], v[30:31], v[102:103] op_sel:[1,0,0]
	s_mov_b64 exec, s[56:57]
	v_pk_fma_f32 v[96:97], v[88:89], v[32:33], v[96:97] op_sel_hi:[0,1,1]
	v_pk_fma_f32 v[98:99], v[88:89], v[34:35], v[98:99] op_sel_hi:[0,1,1]
	s_mov_b64 exec, s[58:59]
	v_pk_fma_f32 v[100:101], v[88:89], v[36:37], v[100:101] op_sel:[1,0,0]
	v_pk_fma_f32 v[102:103], v[88:89], v[38:39], v[102:103] op_sel:[1,0,0]
	s_mov_b64 exec, s[60:61]
	v_pk_fma_f32 v[96:97], v[90:91], v[40:41], v[96:97] op_sel_hi:[0,1,1]
	v_pk_fma_f32 v[98:99], v[90:91], v[42:43], v[98:99] op_sel_hi:[0,1,1]
	s_mov_b64 exec, s[62:63]
	v_pk_fma_f32 v[100:101], v[90:91], v[44:45], v[100:101] op_sel:[1,0,0]
	v_pk_fma_f32 v[102:103], v[90:91], v[46:47], v[102:103] op_sel:[1,0,0]
	s_mov_b64 exec, s[64:65]
	v_pk_fma_f32 v[96:97], v[92:93], v[48:49], v[96:97] op_sel_hi:[0,1,1]
	v_pk_fma_f32 v[98:99], v[92:93], v[50:51], v[98:99] op_sel_hi:[0,1,1]
	s_mov_b64 exec, s[66:67]
	v_pk_fma_f32 v[100:101], v[92:93], v[52:53], v[100:101] op_sel:[1,0,0]
	v_pk_fma_f32 v[102:103], v[92:93], v[54:55], v[102:103] op_sel:[1,0,0]
	s_mov_b64 exec, s[68:69]
	v_pk_fma_f32 v[96:97], v[94:95], v[56:57], v[96:97] op_sel_hi:[0,1,1]
	v_pk_fma_f32 v[98:99], v[94:95], v[58:59], v[98:99] op_sel_hi:[0,1,1]
	s_mov_b64 exec, s[70:71]
	v_pk_fma_f32 v[100:101], v[94:95], v[60:61], v[100:101] op_sel:[1,0,0]
	v_pk_fma_f32 v[102:103], v[94:95], v[62:63], v[102:103] op_sel:[1,0,0]
	s_mov_b64 exec, -1
	v_pk_add_f32 v[96:97], v[96:97], v[100:101]
	v_pk_add_f32 v[98:99], v[98:99], v[102:103]
	s_nop 1
	v_permlane16_swap_b32_e32 v96, v97
	v_permlane16_swap_b32_e32 v98, v99
	v_add_f32_e32 v96, v96, v97
	v_add_f32_e32 v98, v98, v99
	s_nop 1
	v_permlane32_swap_b32_e32 v96, v98
	v_add_f32_e32 v96, v96, v98
	s_waitcnt vmcnt(1)
	v_add_f32_e32 v96, v96, v72
	v_max_f32_e32 v96, 0, v96
	ds_write_b32 v78, v96
	ds_read2_b32 v[80:81], v79 offset0:0 offset1:4
	ds_read2_b32 v[82:83], v79 offset0:8 offset1:12
	ds_read2_b32 v[84:85], v79 offset0:16 offset1:20
	ds_read2_b32 v[86:87], v79 offset0:24 offset1:28
	ds_read2_b32 v[88:89], v79 offset0:32 offset1:36
	ds_read2_b32 v[90:91], v79 offset0:40 offset1:44
	ds_read2_b32 v[92:93], v79 offset0:48 offset1:52
	ds_read2_b32 v[94:95], v79 offset0:56 offset1:60
	s_waitcnt lgkmcnt(0)
	v_cmp_neq_f32_e64 s[40:41], 0, v80
	v_cmp_neq_f32_e64 s[42:43], 0, v81
	v_cmp_neq_f32_e64 s[44:45], 0, v82
	v_cmp_neq_f32_e64 s[46:47], 0, v83
	v_cmp_neq_f32_e64 s[48:49], 0, v84
	v_cmp_neq_f32_e64 s[50:51], 0, v85
	v_cmp_neq_f32_e64 s[52:53], 0, v86
	v_cmp_neq_f32_e64 s[54:55], 0, v87
	v_cmp_neq_f32_e64 s[56:57], 0, v88
	v_cmp_neq_f32_e64 s[58:59], 0, v89
	v_cmp_neq_f32_e64 s[60:61], 0, v90
	v_cmp_neq_f32_e64 s[62:63], 0, v91
	v_cmp_neq_f32_e64 s[64:65], 0, v92
	v_cmp_neq_f32_e64 s[66:67], 0, v93
	v_cmp_neq_f32_e64 s[68:69], 0, v94
	v_cmp_neq_f32_e64 s[70:71], 0, v95
	s_mov_b64 exec, s[40:41]
	global_load_dwordx4 v[0:3], v74, s[14:15] nt
	s_mov_b64 exec, s[42:43]
	global_load_dwordx4 v[4:7], v74, s[14:15] offset:1024 nt
	s_mov_b64 exec, s[44:45]
	global_load_dwordx4 v[8:11], v74, s[14:15] offset:2048 nt
	s_mov_b64 exec, s[46:47]
	global_load_dwordx4 v[12:15], v74, s[14:15] offset:3072 nt
	s_add_u32 s14, s14, 0x1000
	s_addc_u32 s15, s15, 0
	s_mov_b64 exec, s[48:49]
	global_load_dwordx4 v[16:19], v74, s[14:15] nt
	s_mov_b64 exec, s[50:51]
	global_load_dwordx4 v[20:23], v74, s[14:15] offset:1024 nt
	s_mov_b64 exec, s[52:53]
	global_load_dwordx4 v[24:27], v74, s[14:15] offset:2048 nt
	s_mov_b64 exec, s[54:55]
	global_load_dwordx4 v[28:31], v74, s[14:15] offset:3072 nt
	s_add_u32 s14, s14, 0x1000
	s_addc_u32 s15, s15, 0
	s_mov_b64 exec, s[56:57]
	global_load_dwordx4 v[32:35], v74, s[14:15] nt
	s_mov_b64 exec, s[58:59]
	global_load_dwordx4 v[36:39], v74, s[14:15] offset:1024 nt
	s_mov_b64 exec, s[60:61]
	global_load_dwordx4 v[40:43], v74, s[14:15] offset:2048 nt
	s_mov_b64 exec, s[62:63]
	global_load_dwordx4 v[44:47], v74, s[14:15] offset:3072 nt
	s_add_u32 s14, s14, 0x1000
	s_addc_u32 s15, s15, 0
	s_mov_b64 exec, s[64:65]
	global_load_dwordx4 v[48:51], v74, s[14:15] nt
	s_mov_b64 exec, s[66:67]
	global_load_dwordx4 v[52:55], v74, s[14:15] offset:1024 nt
	s_mov_b64 exec, s[68:69]
	global_load_dwordx4 v[56:59], v74, s[14:15] offset:2048 nt
	s_mov_b64 exec, s[70:71]
	global_load_dwordx4 v[60:63], v74, s[14:15] offset:3072 nt
	s_mov_b64 exec, -1
	v_mov_b32_e32 v96, 0
	v_mov_b32_e32 v97, 0
	v_mov_b32_e32 v98, 0
	v_mov_b32_e32 v99, 0
	v_mov_b32_e32 v100, 0
	v_mov_b32_e32 v101, 0
	v_mov_b32_e32 v102, 0
	v_mov_b32_e32 v103, 0
	s_waitcnt vmcnt(0)
	s_mov_b64 exec, s[40:41]
	v_pk_fma_f32 v[96:97], v[80:81], v[0:1], v[96:97] op_sel_hi:[0,1,1]
	v_pk_fma_f32 v[98:99], v[80:81], v[2:3], v[98:99] op_sel_hi:[0,1,1]
	s_mov_b64 exec, s[42:43]
	v_pk_fma_f32 v[100:101], v[80:81], v[4:5], v[100:101] op_sel:[1,0,0]
	v_pk_fma_f32 v[102:103], v[80:81], v[6:7], v[102:103] op_sel:[1,0,0]
	s_mov_b64 exec, s[44:45]
	v_pk_fma_f32 v[96:97], v[82:83], v[8:9], v[96:97] op_sel_hi:[0,1,1]
	v_pk_fma_f32 v[98:99], v[82:83], v[10:11], v[98:99] op_sel_hi:[0,1,1]
	s_mov_b64 exec, s[46:47]
	v_pk_fma_f32 v[100:101], v[82:83], v[12:13], v[100:101] op_sel:[1,0,0]
	v_pk_fma_f32 v[102:103], v[82:83], v[14:15], v[102:103] op_sel:[1,0,0]
	s_mov_b64 exec, s[48:49]
	v_pk_fma_f32 v[96:97], v[84:85], v[16:17], v[96:97] op_sel_hi:[0,1,1]
	v_pk_fma_f32 v[98:99], v[84:85], v[18:19], v[98:99] op_sel_hi:[0,1,1]
	s_mov_b64 exec, s[50:51]
	v_pk_fma_f32 v[100:101], v[84:85], v[20:21], v[100:101] op_sel:[1,0,0]
	v_pk_fma_f32 v[102:103], v[84:85], v[22:23], v[102:103] op_sel:[1,0,0]
	s_mov_b64 exec, s[52:53]
	v_pk_fma_f32 v[96:97], v[86:87], v[24:25], v[96:97] op_sel_hi:[0,1,1]
	v_pk_fma_f32 v[98:99], v[86:87], v[26:27], v[98:99] op_sel_hi:[0,1,1]
	s_mov_b64 exec, s[54:55]
	v_pk_fma_f32 v[100:101], v[86:87], v[28:29], v[100:101] op_sel:[1,0,0]
	v_pk_fma_f32 v[102:103], v[86:87], v[30:31], v[102:103] op_sel:[1,0,0]
	s_mov_b64 exec, s[56:57]
	v_pk_fma_f32 v[96:97], v[88:89], v[32:33], v[96:97] op_sel_hi:[0,1,1]
	v_pk_fma_f32 v[98:99], v[88:89], v[34:35], v[98:99] op_sel_hi:[0,1,1]
	s_mov_b64 exec, s[58:59]
	v_pk_fma_f32 v[100:101], v[88:89], v[36:37], v[100:101] op_sel:[1,0,0]
	v_pk_fma_f32 v[102:103], v[88:89], v[38:39], v[102:103] op_sel:[1,0,0]
	s_mov_b64 exec, s[60:61]
	v_pk_fma_f32 v[96:97], v[90:91], v[40:41], v[96:97] op_sel_hi:[0,1,1]
	v_pk_fma_f32 v[98:99], v[90:91], v[42:43], v[98:99] op_sel_hi:[0,1,1]
	s_mov_b64 exec, s[62:63]
	v_pk_fma_f32 v[100:101], v[90:91], v[44:45], v[100:101] op_sel:[1,0,0]
	v_pk_fma_f32 v[102:103], v[90:91], v[46:47], v[102:103] op_sel:[1,0,0]
	s_mov_b64 exec, s[64:65]
	v_pk_fma_f32 v[96:97], v[92:93], v[48:49], v[96:97] op_sel_hi:[0,1,1]
	v_pk_fma_f32 v[98:99], v[92:93], v[50:51], v[98:99] op_sel_hi:[0,1,1]
	s_mov_b64 exec, s[66:67]
	v_pk_fma_f32 v[100:101], v[92:93], v[52:53], v[100:101] op_sel:[1,0,0]
	v_pk_fma_f32 v[102:103], v[92:93], v[54:55], v[102:103] op_sel:[1,0,0]
	s_mov_b64 exec, s[68:69]
	v_pk_fma_f32 v[96:97], v[94:95], v[56:57], v[96:97] op_sel_hi:[0,1,1]
	v_pk_fma_f32 v[98:99], v[94:95], v[58:59], v[98:99] op_sel_hi:[0,1,1]
	s_mov_b64 exec, s[70:71]
	v_pk_fma_f32 v[100:101], v[94:95], v[60:61], v[100:101] op_sel:[1,0,0]
	v_pk_fma_f32 v[102:103], v[94:95], v[62:63], v[102:103] op_sel:[1,0,0]
	s_mov_b64 exec, -1
	ds_read_b128 v[0:3], v74
	ds_read_b128 v[4:7], v74 offset:1024
	ds_read_b128 v[8:11], v74 offset:2048
	ds_read_b128 v[12:15], v74 offset:3072
	ds_read_b128 v[16:19], v74 offset:4096
	ds_read_b128 v[20:23], v74 offset:5120
	ds_read_b128 v[24:27], v74 offset:6144
	ds_read_b128 v[28:31], v74 offset:7168
	ds_read_b128 v[32:35], v74 offset:8192
	ds_read_b128 v[36:39], v74 offset:9216
	ds_read_b128 v[40:43], v74 offset:10240
	ds_read_b128 v[44:47], v74 offset:11264
	ds_read_b128 v[48:51], v74 offset:12288
	ds_read_b128 v[52:55], v74 offset:13312
	ds_read_b128 v[56:59], v74 offset:14336
	v_pk_add_f32 v[96:97], v[96:97], v[100:101]
	v_pk_add_f32 v[98:99], v[98:99], v[102:103]
	s_nop 1
	v_permlane16_swap_b32_e32 v96, v97
	v_permlane16_swap_b32_e32 v98, v99
	v_add_f32_e32 v96, v96, v97
	v_add_f32_e32 v98, v98, v99
	s_nop 1
	v_permlane32_swap_b32_e32 v96, v98
	v_add_f32_e32 v96, v96, v98
	v_add_f32_e32 v96, v96, v73
	s_waitcnt lgkmcnt(5)
	ds_read_b128 v[60:63], v74 offset:15360
	ds_write_b32 v78, v96
	ds_read2_b32 v[80:81], v79 offset0:0 offset1:4
	ds_read2_b32 v[82:83], v79 offset0:8 offset1:12
	ds_read2_b32 v[84:85], v79 offset0:16 offset1:20
	ds_read2_b32 v[86:87], v79 offset0:24 offset1:28
	ds_read2_b32 v[88:89], v79 offset0:32 offset1:36
	ds_read2_b32 v[90:91], v79 offset0:40 offset1:44
	ds_read2_b32 v[92:93], v79 offset0:48 offset1:52
	ds_read2_b32 v[94:95], v79 offset0:56 offset1:60
	v_lshlrev_b32_e32 v72, 3, v76
	v_lshl_or_b32 v72, v75, 2, v72
	v_cmp_gt_u32_e32 vcc, 2, v75
	s_waitcnt lgkmcnt(0)
	v_pk_mul_f32 v[96:97], v[80:81], v[0:1] op_sel_hi:[0,1]
	v_pk_mul_f32 v[98:99], v[80:81], v[2:3] op_sel_hi:[0,1]
	v_pk_mul_f32 v[100:101], v[80:81], v[4:5] op_sel:[1,0]
	v_pk_mul_f32 v[102:103], v[80:81], v[6:7] op_sel:[1,0]
	v_pk_fma_f32 v[96:97], v[82:83], v[8:9], v[96:97] op_sel_hi:[0,1,1]
	v_pk_fma_f32 v[98:99], v[82:83], v[10:11], v[98:99] op_sel_hi:[0,1,1]
	v_pk_fma_f32 v[100:101], v[82:83], v[12:13], v[100:101] op_sel:[1,0,0]
	v_pk_fma_f32 v[102:103], v[82:83], v[14:15], v[102:103] op_sel:[1,0,0]
	v_pk_fma_f32 v[96:97], v[84:85], v[16:17], v[96:97] op_sel_hi:[0,1,1]
	v_pk_fma_f32 v[98:99], v[84:85], v[18:19], v[98:99] op_sel_hi:[0,1,1]
	v_pk_fma_f32 v[100:101], v[84:85], v[20:21], v[100:101] op_sel:[1,0,0]
	v_pk_fma_f32 v[102:103], v[84:85], v[22:23], v[102:103] op_sel:[1,0,0]
	v_pk_fma_f32 v[96:97], v[86:87], v[24:25], v[96:97] op_sel_hi:[0,1,1]
	v_pk_fma_f32 v[98:99], v[86:87], v[26:27], v[98:99] op_sel_hi:[0,1,1]
	v_pk_fma_f32 v[100:101], v[86:87], v[28:29], v[100:101] op_sel:[1,0,0]
	v_pk_fma_f32 v[102:103], v[86:87], v[30:31], v[102:103] op_sel:[1,0,0]
	v_pk_fma_f32 v[96:97], v[88:89], v[32:33], v[96:97] op_sel_hi:[0,1,1]
	v_pk_fma_f32 v[98:99], v[88:89], v[34:35], v[98:99] op_sel_hi:[0,1,1]
	v_pk_fma_f32 v[100:101], v[88:89], v[36:37], v[100:101] op_sel:[1,0,0]
	v_pk_fma_f32 v[102:103], v[88:89], v[38:39], v[102:103] op_sel:[1,0,0]
	v_pk_fma_f32 v[96:97], v[90:91], v[40:41], v[96:97] op_sel_hi:[0,1,1]
	v_pk_fma_f32 v[98:99], v[90:91], v[42:43], v[98:99] op_sel_hi:[0,1,1]
	v_pk_fma_f32 v[100:101], v[90:91], v[44:45], v[100:101] op_sel:[1,0,0]
	v_pk_fma_f32 v[102:103], v[90:91], v[46:47], v[102:103] op_sel:[1,0,0]
	v_pk_fma_f32 v[96:97], v[92:93], v[48:49], v[96:97] op_sel_hi:[0,1,1]
	v_pk_fma_f32 v[98:99], v[92:93], v[50:51], v[98:99] op_sel_hi:[0,1,1]
	v_pk_fma_f32 v[100:101], v[92:93], v[52:53], v[100:101] op_sel:[1,0,0]
	v_pk_fma_f32 v[102:103], v[92:93], v[54:55], v[102:103] op_sel:[1,0,0]
	v_pk_fma_f32 v[96:97], v[94:95], v[56:57], v[96:97] op_sel_hi:[0,1,1]
	v_pk_fma_f32 v[98:99], v[94:95], v[58:59], v[98:99] op_sel_hi:[0,1,1]
	v_pk_fma_f32 v[100:101], v[94:95], v[60:61], v[100:101] op_sel:[1,0,0]
	v_pk_fma_f32 v[102:103], v[94:95], v[62:63], v[102:103] op_sel:[1,0,0]
	v_pk_add_f32 v[96:97], v[96:97], v[100:101]
	v_pk_add_f32 v[98:99], v[98:99], v[102:103]
	s_nop 1
	v_permlane16_swap_b32_e32 v96, v98
	v_permlane16_swap_b32_e32 v97, v99
	v_add_f32_e32 v96, v96, v98
	v_add_f32_e32 v97, v97, v99
	v_mov_b32_e32 v80, v96
	v_mov_b32_e32 v81, v97
	s_nop 1
	v_permlane32_swap_b32_e32 v96, v80
	v_permlane32_swap_b32_e32 v97, v81
	v_add_f32_e32 v96, v96, v80
	v_add_f32_e32 v97, v97, v81
	v_cvt_pk_f16_f32 v73, v96, v97
	s_and_saveexec_b64 s[4:5], vcc
	global_atomic_pk_add_f16 v72, v73, s[20:21]
	s_endpgm
	.p2align	8
